# hybrid K1 ring 32 + slot requests for the queued entries issued at the start of the last chunk (queue reset fixed)
# speedup vs baseline: 1.0356x; 1.0356x over previous
.Lk1_scan:
	s_load_dwordx2 s[4:5], s[0:1], 0x0
	s_load_dwordx4 s[8:11], s[0:1], 0x20
	s_load_dwordx2 s[12:13], s[0:1], 0x30
	v_and_b32_e32 v6, 63, v0
	v_readfirstlane_b32 s3, v0
	v_lshlrev_b32_e32 v1, 4, v6
	v_lshlrev_b32_e32 v2, 2, v6
	v_or_b32_e32 v3, 1, v2
	v_or_b32_e32 v4, 2, v2
	v_or_b32_e32 v5, 3, v2
	s_lshr_b32 s3, s3, 6
	s_sub_u32 s16, s2, 0x60
	s_lshl_b32 s16, s16, 2
	s_add_u32 s16, s16, s3
	s_mul_i32 s17, s16, 0x48000
	s_lshr_b32 s18, s17, 2
	s_lshl_b32 s24, s3, 13
	s_mov_b32 s25, s24
	s_mov_b32 s28, s24
	s_mov_b32 s36, 0
	s_mov_b64 s[62:63], 0
	v_mov_b32_e32 v21, 1
	s_mov_b32 s27, 0
	s_mov_b32 s29, 0x55555556
	s_mov_b32 s31, 0xc0000
	s_waitcnt lgkmcnt(0)
	s_and_b32 s50, s16, 15
	s_mul_i32 s52, s50, 256
	s_add_u32 s52, s52, 14336
	s_lshl_b32 s53, s50, 6
	s_add_u32 s53, s53, 0xe000
	s_add_u32 s54, s10, s53
	s_addc_u32 s55, s11, 0
	s_mul_i32 s59, s16, 7
	s_mul_i32 s57, s59, 0x8000
	s_lshr_b32 s18, s57, 2
	s_add_u32 s6, s4, s57
	s_addc_u32 s7, s5, 0
	v_mov_b32_e32 v27, 0
	global_load_dwordx4 v[28:31], v1, s[6:7] nt
	s_add_u32 s6, s6, 0x400
	s_addc_u32 s7, s7, 0
	global_load_dwordx4 v[32:35], v1, s[6:7] nt
	s_add_u32 s6, s6, 0x400
	s_addc_u32 s7, s7, 0
	global_load_dwordx4 v[36:39], v1, s[6:7] nt
	s_add_u32 s6, s6, 0x400
	s_addc_u32 s7, s7, 0
	global_load_dwordx4 v[40:43], v1, s[6:7] nt
	s_add_u32 s6, s6, 0x400
	s_addc_u32 s7, s7, 0
	global_load_dwordx4 v[44:47], v1, s[6:7] nt
	s_add_u32 s6, s6, 0x400
	s_addc_u32 s7, s7, 0
	global_load_dwordx4 v[48:51], v1, s[6:7] nt
	s_add_u32 s6, s6, 0x400
	s_addc_u32 s7, s7, 0
	global_load_dwordx4 v[52:55], v1, s[6:7] nt
	s_add_u32 s6, s6, 0x400
	s_addc_u32 s7, s7, 0
	global_load_dwordx4 v[56:59], v1, s[6:7] nt
	s_add_u32 s6, s6, 0x400
	s_addc_u32 s7, s7, 0
	global_load_dwordx4 v[60:63], v1, s[6:7] nt
	s_add_u32 s6, s6, 0x400
	s_addc_u32 s7, s7, 0
	global_load_dwordx4 v[64:67], v1, s[6:7] nt
	s_add_u32 s6, s6, 0x400
	s_addc_u32 s7, s7, 0
	global_load_dwordx4 v[68:71], v1, s[6:7] nt
	s_add_u32 s6, s6, 0x400
	s_addc_u32 s7, s7, 0
	global_load_dwordx4 v[72:75], v1, s[6:7] nt
	s_add_u32 s6, s6, 0x400
	s_addc_u32 s7, s7, 0
	global_load_dwordx4 v[76:79], v1, s[6:7] nt
	s_add_u32 s6, s6, 0x400
	s_addc_u32 s7, s7, 0
	global_load_dwordx4 v[80:83], v1, s[6:7] nt
	s_add_u32 s6, s6, 0x400
	s_addc_u32 s7, s7, 0
	global_load_dwordx4 v[84:87], v1, s[6:7] nt
	s_add_u32 s6, s6, 0x400
	s_addc_u32 s7, s7, 0
	global_load_dwordx4 v[88:91], v1, s[6:7] nt
	s_add_u32 s6, s6, 0x400
	s_addc_u32 s7, s7, 0
	global_load_dwordx4 v[92:95], v1, s[6:7] nt
	s_add_u32 s6, s6, 0x400
	s_addc_u32 s7, s7, 0
	global_load_dwordx4 v[96:99], v1, s[6:7] nt
	s_add_u32 s6, s6, 0x400
	s_addc_u32 s7, s7, 0
	global_load_dwordx4 v[100:103], v1, s[6:7] nt
	s_add_u32 s6, s6, 0x400
	s_addc_u32 s7, s7, 0
	global_load_dwordx4 v[104:107], v1, s[6:7] nt
	s_add_u32 s6, s6, 0x400
	s_addc_u32 s7, s7, 0
	global_load_dwordx4 v[108:111], v1, s[6:7] nt
	s_add_u32 s6, s6, 0x400
	s_addc_u32 s7, s7, 0
	global_load_dwordx4 v[112:115], v1, s[6:7] nt
	s_add_u32 s6, s6, 0x400
	s_addc_u32 s7, s7, 0
	global_load_dwordx4 v[116:119], v1, s[6:7] nt
	s_add_u32 s6, s6, 0x400
	s_addc_u32 s7, s7, 0
	global_load_dwordx4 v[120:123], v1, s[6:7] nt
	s_add_u32 s6, s6, 0x400
	s_addc_u32 s7, s7, 0
	global_load_dwordx4 v[124:127], v1, s[6:7] nt
	s_add_u32 s6, s6, 0x400
	s_addc_u32 s7, s7, 0
	global_load_dwordx4 v[128:131], v1, s[6:7] nt
	s_add_u32 s6, s6, 0x400
	s_addc_u32 s7, s7, 0
	global_load_dwordx4 v[132:135], v1, s[6:7] nt
	s_add_u32 s6, s6, 0x400
	s_addc_u32 s7, s7, 0
	global_load_dwordx4 v[136:139], v1, s[6:7] nt
	s_add_u32 s6, s6, 0x400
	s_addc_u32 s7, s7, 0
	global_load_dwordx4 v[140:143], v1, s[6:7] nt
	s_add_u32 s6, s6, 0x400
	s_addc_u32 s7, s7, 0
	global_load_dwordx4 v[144:147], v1, s[6:7] nt
	s_add_u32 s6, s6, 0x400
	s_addc_u32 s7, s7, 0
	global_load_dwordx4 v[148:151], v1, s[6:7] nt
	s_add_u32 s6, s6, 0x400
	s_addc_u32 s7, s7, 0
	global_load_dwordx4 v[152:155], v1, s[6:7] nt
	s_add_u32 s6, s6, 0x400
	s_addc_u32 s7, s7, 0
	s_mov_b32 s26, 9
	s_add_u32 s57, s59, 1
	s_mul_i32 s57, s57, 0x8000
	s_lshr_b32 s58, s57, 2
	s_add_u32 s6, s4, s57
	s_addc_u32 s7, s5, 0
	s_mov_b32 s26, 0

.Lk1_noreq:
	s_add_u32 s26, s26, 1
	s_branch .Lk1_main
.Lk1_lastchunk:
	s_cmp_ge_u32 s28, s25
	s_cbranch_scc1 .Lk1_inone_l
	s_waitcnt lgkmcnt(0)
	v_lshl_add_u32 v25, v6, 3, s28
	v_cmp_gt_u32_e32 vcc, s25, v25
	s_and_saveexec_b64 s[32:33], vcc
	s_mov_b64 s[34:35], exec
	ds_read_b64 v[16:17], v25
	s_waitcnt lgkmcnt(0)
	v_lshrrev_b32_e32 v23, 12, v16
	v_mul_hi_u32 v23, v23, s29
	v_mul_u32_u24_e32 v19, 0x3000, v23
	v_sub_u32_e32 v19, v16, v19
	v_lshlrev_b32_e32 v20, 2, v19
	global_atomic_add v22, v20, v21, s[8:9] sc0
	global_atomic_add_f32 v20, v17, s[10:11]
	v_mov_b32_e32 v16, v23
	s_mov_b64 exec, -1
	s_mov_b32 s36, 1
	s_add_u32 s28, s28, 0x200
	s_cmp_ge_u32 s28, s25
	s_cbranch_scc0 .Lk1_inone_l
	s_mov_b32 s28, s24
	s_mov_b32 s25, s24
.Lk1_inone_l:
	s_cmp_ge_u32 s28, s25
	s_cbranch_scc1 .Lk1_inone_lx
	s_waitcnt lgkmcnt(0)
	v_lshl_add_u32 v25, v6, 3, s28
	v_cmp_gt_u32_e32 vcc, s25, v25
	s_and_saveexec_b64 s[32:33], vcc
	s_mov_b64 s[62:63], exec
	ds_read_b64 v[156:157], v25
	s_waitcnt lgkmcnt(0)
	v_lshrrev_b32_e32 v161, 12, v156
	v_mul_hi_u32 v161, v161, s29
	v_mul_u32_u24_e32 v158, 0x3000, v161
	v_sub_u32_e32 v158, v156, v158
	v_lshlrev_b32_e32 v159, 2, v158
	global_atomic_add v160, v159, v21, s[8:9] sc0
	global_atomic_add_f32 v159, v157, s[10:11]
	v_mov_b32_e32 v156, v161
	s_mov_b64 exec, -1
	s_add_u32 s28, s28, 0x200
	s_cmp_ge_u32 s28, s25
	s_cbranch_scc0 .Lk1_inone_lx
	s_mov_b32 s28, s24
	s_mov_b32 s25, s24

.Lk1_cskip_fin_pend:
	s_mov_b64 exec, s[62:63]
	s_cbranch_execz .Lk1_cskip_fin_x
	v_mul_u32_u24_e32 v162, 0x3000, v158
	v_lshlrev_b32_e32 v161, 6, v158
	v_cmp_gt_u32_e32 vcc, 64, v160
	v_add_u32_e32 v161, v161, v160
	v_add3_u32 v162, v162, v160, s31
	v_cndmask_b32_e32 v161, v162, v161, vcc
	v_lshlrev_b32_e32 v161, 3, v161
	global_store_dwordx2 v161, v[156:157], s[12:13]
.Lk1_cskip_fin_x:
	s_mov_b64 exec, -1
	s_mov_b64 s[62:63], 0
	s_mov_b64 s[40:41], 0
	s_mov_b64 s[42:43], 0
	s_mov_b64 s[44:45], 0
	s_mov_b64 s[46:47], 0
	s_cmp_ge_u32 s28, s25
	s_cbranch_scc1 .Lk1_inone_fin0
	s_waitcnt lgkmcnt(0)
	v_lshl_add_u32 v25, v6, 3, s28
	v_cmp_gt_u32_e32 vcc, s25, v25
	s_and_saveexec_b64 s[32:33], vcc
	s_mov_b64 s[40:41], exec
	ds_read_b64 v[28:29], v25
	s_waitcnt lgkmcnt(0)
	v_lshrrev_b32_e32 v33, 12, v28
	v_mul_hi_u32 v33, v33, s29
	v_mul_u32_u24_e32 v30, 0x3000, v33
	v_sub_u32_e32 v30, v28, v30
	v_lshlrev_b32_e32 v31, 2, v30
	global_atomic_add v32, v31, v21, s[8:9] sc0
	global_atomic_add_f32 v31, v29, s[10:11]
	v_mov_b32_e32 v28, v33
	s_mov_b64 exec, -1
	s_add_u32 s28, s28, 0x200

	.amdhsa_kernel _Z9k1_kernelPKfS0_S0_PDF16_PiPfP15HIP_vector_typeIiLj2EES6_
		.amdhsa_group_segment_fixed_size 37392
		.amdhsa_private_segment_fixed_size 0
		.amdhsa_kernarg_size 64
		.amdhsa_user_sgpr_count 2
		.amdhsa_user_sgpr_dispatch_ptr 0
		.amdhsa_user_sgpr_queue_ptr 0
		.amdhsa_user_sgpr_kernarg_segment_ptr 1
		.amdhsa_user_sgpr_dispatch_id 0
		.amdhsa_user_sgpr_kernarg_preload_length 0
		.amdhsa_user_sgpr_kernarg_preload_offset 0
		.amdhsa_user_sgpr_private_segment_size 0
		.amdhsa_uses_dynamic_stack 0
		.amdhsa_enable_private_segment 0
		.amdhsa_system_sgpr_workgroup_id_x 1
		.amdhsa_system_sgpr_workgroup_id_y 0
		.amdhsa_system_sgpr_workgroup_id_z 0
		.amdhsa_system_sgpr_workgroup_info 0
		.amdhsa_system_vgpr_workitem_id 0
		.amdhsa_next_free_vgpr 163
		.amdhsa_next_free_sgpr 96
		.amdhsa_accum_offset 164
		.amdhsa_reserve_vcc 1
		.amdhsa_float_round_mode_32 0
		.amdhsa_float_round_mode_16_64 0
		.amdhsa_float_denorm_mode_32 3
		.amdhsa_float_denorm_mode_16_64 3
		.amdhsa_dx10_clamp 1
		.amdhsa_ieee_mode 1
		.amdhsa_fp16_overflow 0
		.amdhsa_tg_split 0
		.amdhsa_exception_fp_ieee_invalid_op 0
		.amdhsa_exception_fp_denorm_src 0
		.amdhsa_exception_fp_ieee_div_zero 0
		.amdhsa_exception_fp_ieee_overflow 0
		.amdhsa_exception_fp_ieee_underflow 0
		.amdhsa_exception_fp_ieee_inexact 0
		.amdhsa_exception_int_div_zero 0
	.end_amdhsa_kernel

.Lfunc_end0:
	.size	_Z9k1_kernelPKfS0_S0_PDF16_PiPfP15HIP_vector_typeIiLj2EES6_, .Lfunc_end0-_Z9k1_kernelPKfS0_S0_PDF16_PiPfP15HIP_vector_typeIiLj2EES6_
	.set _Z9k1_kernelPKfS0_S0_PDF16_PiPfP15HIP_vector_typeIiLj2EES6_.num_vgpr, 163
	.set _Z9k1_kernelPKfS0_S0_PDF16_PiPfP15HIP_vector_typeIiLj2EES6_.num_agpr, 0
	.set _Z9k1_kernelPKfS0_S0_PDF16_PiPfP15HIP_vector_typeIiLj2EES6_.numbered_sgpr, 26
	.set _Z9k1_kernelPKfS0_S0_PDF16_PiPfP15HIP_vector_typeIiLj2EES6_.num_named_barrier, 0
	.set _Z9k1_kernelPKfS0_S0_PDF16_PiPfP15HIP_vector_typeIiLj2EES6_.private_seg_size, 0
	.set _Z9k1_kernelPKfS0_S0_PDF16_PiPfP15HIP_vector_typeIiLj2EES6_.uses_vcc, 1
	.set _Z9k1_kernelPKfS0_S0_PDF16_PiPfP15HIP_vector_typeIiLj2EES6_.uses_flat_scratch, 0
	.set _Z9k1_kernelPKfS0_S0_PDF16_PiPfP15HIP_vector_typeIiLj2EES6_.has_dyn_sized_stack, 0
	.set _Z9k1_kernelPKfS0_S0_PDF16_PiPfP15HIP_vector_typeIiLj2EES6_.has_recursion, 0
	.set _Z9k1_kernelPKfS0_S0_PDF16_PiPfP15HIP_vector_typeIiLj2EES6_.has_indirect_call, 0

amdhsa.kernels:
  - .agpr_count:     0
    .args:
      - .actual_access:  read_only
        .address_space:  global
        .offset:         0
        .size:           8
        .value_kind:     global_buffer
      - .actual_access:  read_only
        .address_space:  global
        .offset:         8
        .size:           8
        .value_kind:     global_buffer
      - .actual_access:  read_only
        .address_space:  global
        .offset:         16
        .size:           8
        .value_kind:     global_buffer
      - .actual_access:  write_only
        .address_space:  global
        .offset:         24
        .size:           8
        .value_kind:     global_buffer
      - .address_space:  global
        .offset:         32
        .size:           8
        .value_kind:     global_buffer
      - .address_space:  global
        .offset:         40
        .size:           8
        .value_kind:     global_buffer
      - .actual_access:  write_only
        .address_space:  global
        .offset:         48
        .size:           8
        .value_kind:     global_buffer
      - .actual_access:  write_only
        .address_space:  global
        .offset:         56
        .size:           8
        .value_kind:     global_buffer
    .group_segment_fixed_size: 37392
    .kernarg_segment_align: 8
    .kernarg_segment_size: 64
    .language:       OpenCL C
    .language_version:
      - 2
      - 0
    .max_flat_workgroup_size: 256
    .name:           _Z9k1_kernelPKfS0_S0_PDF16_PiPfP15HIP_vector_typeIiLj2EES6_
    .private_segment_fixed_size: 0
    .sgpr_count:     32
    .sgpr_spill_count: 0
    .symbol:         _Z9k1_kernelPKfS0_S0_PDF16_PiPfP15HIP_vector_typeIiLj2EES6_.kd
    .uniform_work_group_size: 1
    .uses_dynamic_stack: false
    .vgpr_count:     163
    .vgpr_spill_count: 0
    .wavefront_size: 64
  - .agpr_count:     0
    .args:
      - .actual_access:  read_only
        .address_space:  global
        .offset:         0
        .size:           8
        .value_kind:     global_buffer
      - .actual_access:  read_only
        .address_space:  global
        .offset:         8
        .size:           8
        .value_kind:     global_buffer
      - .actual_access:  read_only
        .address_space:  global
        .offset:         16
        .size:           8
        .value_kind:     global_buffer
      - .actual_access:  read_only
        .address_space:  global
        .offset:         24
        .size:           8
        .value_kind:     global_buffer
      - .actual_access:  read_only
        .address_space:  global
        .offset:         32
        .size:           8
        .value_kind:     global_buffer
      - .actual_access:  read_only
        .address_space:  global
        .offset:         40
        .size:           8
        .value_kind:     global_buffer
      - .actual_access:  read_only
        .address_space:  global
        .offset:         48
        .size:           8
        .value_kind:     global_buffer
      - .actual_access:  read_only
        .address_space:  global
        .offset:         56
        .size:           8
        .value_kind:     global_buffer
      - .actual_access:  read_only
        .address_space:  global
        .offset:         64
        .size:           8
        .value_kind:     global_buffer
      - .actual_access:  write_only
        .address_space:  global
        .offset:         72
        .size:           8
        .value_kind:     global_buffer
      - .address_space:  global
        .offset:         80
        .size:           8
        .value_kind:     global_buffer
    .group_segment_fixed_size: 44224
    .kernarg_segment_align: 8
    .kernarg_segment_size: 88
    .language:       OpenCL C
    .language_version:
      - 2
      - 0
    .max_flat_workgroup_size: 512
    .name:           _Z11agg2_kernelPKiPKfPK15HIP_vector_typeIiLj2EEPKDF16_S2_S2_S2_S2_S2_PfS9_
    .private_segment_fixed_size: 0
    .sgpr_count:     41
    .sgpr_spill_count: 0
    .symbol:         _Z11agg2_kernelPKiPKfPK15HIP_vector_typeIiLj2EEPKDF16_S2_S2_S2_S2_S2_PfS9_.kd
    .uniform_work_group_size: 1
    .uses_dynamic_stack: false
    .vgpr_count:     80
    .vgpr_spill_count: 0
    .wavefront_size: 64
  - .agpr_count:     0
    .args:
      - .actual_access:  read_only
        .address_space:  global
        .offset:         0
        .size:           8
        .value_kind:     global_buffer
      - .actual_access:  read_only
        .address_space:  global
        .offset:         8
        .size:           8
        .value_kind:     global_buffer
      - .actual_access:  read_only
        .address_space:  global
        .offset:         16
        .size:           8
        .value_kind:     global_buffer
      - .actual_access:  read_only
        .address_space:  global
        .offset:         24
        .size:           8
        .value_kind:     global_buffer
      - .actual_access:  write_only
        .address_space:  global
        .offset:         32
        .size:           8
        .value_kind:     global_buffer
      - .offset:         40
        .size:           4
        .value_kind:     hidden_block_count_x
      - .offset:         44
        .size:           4
        .value_kind:     hidden_block_count_y
      - .offset:         48
        .size:           4
        .value_kind:     hidden_block_count_z
      - .offset:         52
        .size:           2
        .value_kind:     hidden_group_size_x
      - .offset:         54
        .size:           2
        .value_kind:     hidden_group_size_y
      - .offset:         56
        .size:           2
        .value_kind:     hidden_group_size_z
      - .offset:         58
        .size:           2
        .value_kind:     hidden_remainder_x
      - .offset:         60
        .size:           2
        .value_kind:     hidden_remainder_y
      - .offset:         62
        .size:           2
        .value_kind:     hidden_remainder_z
      - .offset:         80
        .size:           8
        .value_kind:     hidden_global_offset_x
      - .offset:         88
        .size:           8
        .value_kind:     hidden_global_offset_y
      - .offset:         96
        .size:           8
        .value_kind:     hidden_global_offset_z
      - .offset:         104
        .size:           2
        .value_kind:     hidden_grid_dims
    .group_segment_fixed_size: 512
    .kernarg_segment_align: 8
    .kernarg_segment_size: 296
    .language:       OpenCL C
    .language_version:
      - 2
      - 0
    .max_flat_workgroup_size: 256
    .name:           _Z12final_kernelPKfS0_S0_S0_Pf
    .private_segment_fixed_size: 0
    .sgpr_count:     22
    .sgpr_spill_count: 0
    .symbol:         _Z12final_kernelPKfS0_S0_S0_Pf.kd
    .uniform_work_group_size: 1
    .uses_dynamic_stack: false
    .vgpr_count:     49
    .vgpr_spill_count: 0
    .wavefront_size: 64
  - .agpr_count:     0
    .args:
      - .actual_access:  read_only
        .address_space:  global
        .offset:         0
        .size:           8
        .value_kind:     global_buffer
      - .actual_access:  read_only
        .address_space:  global
        .offset:         8
        .size:           8
        .value_kind:     global_buffer
      - .address_space:  global
        .offset:         16
        .size:           8
        .value_kind:     global_buffer
      - .address_space:  global
        .offset:         24
        .size:           8
        .value_kind:     global_buffer
      - .actual_access:  read_only
        .address_space:  global
        .offset:         32
        .size:           8
        .value_kind:     global_buffer
      - .actual_access:  read_only
        .address_space:  global
        .offset:         40
        .size:           8
        .value_kind:     global_buffer
      - .actual_access:  write_only
        .address_space:  global
        .offset:         48
        .size:           8
        .value_kind:     global_buffer
      - .address_space:  global
        .offset:         56
        .size:           8
        .value_kind:     global_buffer
    .group_segment_fixed_size: 8192
    .kernarg_segment_align: 8
    .kernarg_segment_size: 64
    .language:       OpenCL C
    .language_version:
      - 2
      - 0
    .max_flat_workgroup_size: 512
    .name:           _Z10agg_kernelILi128ELb1EEvPKiPKfP15HIP_vector_typeIiLj2EES6_PKDF16_S3_PDF16_Pf
    .private_segment_fixed_size: 0
    .sgpr_count:     42
    .sgpr_spill_count: 0
    .symbol:         _Z10agg_kernelILi128ELb1EEvPKiPKfP15HIP_vector_typeIiLj2EES6_PKDF16_S3_PDF16_Pf.kd
    .uniform_work_group_size: 1
    .uses_dynamic_stack: false
    .vgpr_count:     80
    .vgpr_spill_count: 0
    .wavefront_size: 64
